# v45 + out-projection GEMM epilogue rewritten: x residual loads run six steps ahead in dead fragment registers with counted vmcnt instead of a 16-step load->vmcnt(0)->store ladder
# speedup vs baseline: 1.0199x; 1.0004x over previous
.LBB0_412:
	v_lshl_add_u32 v146, s24, 8, v148
	v_lshl_add_u32 v144, s56, 8, v158
	v_ashrrev_i32_e32 v147, 31, v146
	v_ashrrev_i32_e32 v145, 31, v144
	v_lshlrev_b64 v[162:163], 10, v[146:147]
	v_lshl_add_u64 v[170:171], v[162:163], 0, v[144:145]
	v_lshl_add_u64 v[172:173], v[170:171], 2, s[8:9]
	v_lshl_add_u64 v[170:171], v[170:171], 1, s[10:11]
	s_andn2_b64 vcc, exec, s[0:1]
	s_mov_b64 s[0:1], -1
	s_mov_b32 s71, 0
	s_mov_b32 s73, 0
	global_load_dwordx4 v[174:177], v[172:173], off
	global_load_dwordx4 v[178:181], v[172:173], off offset:16
	global_load_dwordx4 v[182:185], v[172:173], off offset:512
	global_load_dwordx4 v[186:189], v[172:173], off offset:528
	s_mov_b32 s70, 0x10000
	v_lshl_add_u64 v[224:225], v[172:173], 0, s[70:71]
	global_load_dwordx4 v[190:193], v[224:225], off
	global_load_dwordx4 v[194:197], v[224:225], off offset:16
	global_load_dwordx4 v[198:201], v[224:225], off offset:512
	global_load_dwordx4 v[202:205], v[224:225], off offset:528
	s_mov_b32 s70, 0x20000
	v_lshl_add_u64 v[226:227], v[172:173], 0, s[70:71]
	global_load_dwordx4 v[206:209], v[226:227], off
	global_load_dwordx4 v[210:213], v[226:227], off offset:16
	global_load_dwordx4 v[214:217], v[226:227], off offset:512
	global_load_dwordx4 v[218:221], v[226:227], off offset:528
	s_mov_b32 s70, 0x30000
	v_lshl_add_u64 v[228:229], v[172:173], 0, s[70:71]
	s_mov_b32 s70, 0x80000
	v_lshl_add_u64 v[230:231], v[172:173], 0, s[70:71]
	s_mov_b32 s70, 0x90000
	v_lshl_add_u64 v[232:233], v[172:173], 0, s[70:71]
	s_mov_b32 s70, 0xa0000
	v_lshl_add_u64 v[234:235], v[172:173], 0, s[70:71]
	s_mov_b32 s70, 0xb0000
	v_lshl_add_u64 v[236:237], v[172:173], 0, s[70:71]
	s_mov_b32 s72, 0x8000
	v_lshl_add_u64 v[240:241], v[170:171], 0, s[72:73]
	s_mov_b32 s72, 0x10000
	v_lshl_add_u64 v[242:243], v[170:171], 0, s[72:73]
	s_mov_b32 s72, 0x18000
	v_lshl_add_u64 v[244:245], v[170:171], 0, s[72:73]
	s_mov_b32 s72, 0x40000
	v_lshl_add_u64 v[246:247], v[170:171], 0, s[72:73]
	s_mov_b32 s72, 0x48000
	v_lshl_add_u64 v[248:249], v[170:171], 0, s[72:73]
	s_mov_b32 s72, 0x50000
	v_lshl_add_u64 v[250:251], v[170:171], 0, s[72:73]
	s_mov_b32 s72, 0x58000
	v_lshl_add_u64 v[252:253], v[170:171], 0, s[72:73]
	s_waitcnt vmcnt(10)
	v_pk_add_f32 v[124:125], v[124:125], v[174:175]
	v_pk_add_f32 v[126:127], v[126:127], v[176:177]
	v_pk_add_f32 v[120:121], v[120:121], v[178:179]
	v_pk_add_f32 v[122:123], v[122:123], v[180:181]
	v_cvt_pk_bf16_f32 v124, v124, v125
	v_cvt_pk_bf16_f32 v125, v126, v127
	v_cvt_pk_bf16_f32 v126, v120, v121
	v_cvt_pk_bf16_f32 v127, v122, v123
	global_store_dwordx4 v[170:171], v[124:127], off
	global_load_dwordx4 v[174:177], v[228:229], off
	global_load_dwordx4 v[178:181], v[228:229], off offset:16
	s_waitcnt vmcnt(11)
	v_pk_add_f32 v[116:117], v[116:117], v[182:183]
	v_pk_add_f32 v[118:119], v[118:119], v[184:185]
	v_pk_add_f32 v[112:113], v[112:113], v[186:187]
	v_pk_add_f32 v[114:115], v[114:115], v[188:189]
	v_cvt_pk_bf16_f32 v116, v116, v117
	v_cvt_pk_bf16_f32 v117, v118, v119
	v_cvt_pk_bf16_f32 v118, v112, v113
	v_cvt_pk_bf16_f32 v119, v114, v115
	global_store_dwordx4 v[170:171], v[116:119], off offset:256
	global_load_dwordx4 v[182:185], v[228:229], off offset:512
	global_load_dwordx4 v[186:189], v[228:229], off offset:528
	s_waitcnt vmcnt(12)
	v_pk_add_f32 v[108:109], v[108:109], v[190:191]
	v_pk_add_f32 v[110:111], v[110:111], v[192:193]
	v_pk_add_f32 v[104:105], v[104:105], v[194:195]
	v_pk_add_f32 v[106:107], v[106:107], v[196:197]
	v_cvt_pk_bf16_f32 v108, v108, v109
	v_cvt_pk_bf16_f32 v109, v110, v111
	v_cvt_pk_bf16_f32 v110, v104, v105
	v_cvt_pk_bf16_f32 v111, v106, v107
	global_store_dwordx4 v[240:241], v[108:111], off
	global_load_dwordx4 v[190:193], v[230:231], off
	global_load_dwordx4 v[194:197], v[230:231], off offset:16
	s_waitcnt vmcnt(13)
	v_pk_add_f32 v[100:101], v[100:101], v[198:199]
	v_pk_add_f32 v[102:103], v[102:103], v[200:201]
	v_pk_add_f32 v[96:97], v[96:97], v[202:203]
	v_pk_add_f32 v[98:99], v[98:99], v[204:205]
	v_cvt_pk_bf16_f32 v100, v100, v101
	v_cvt_pk_bf16_f32 v101, v102, v103
	v_cvt_pk_bf16_f32 v102, v96, v97
	v_cvt_pk_bf16_f32 v103, v98, v99
	global_store_dwordx4 v[240:241], v[100:103], off offset:256
	global_load_dwordx4 v[198:201], v[230:231], off offset:512
	global_load_dwordx4 v[202:205], v[230:231], off offset:528
	s_waitcnt vmcnt(14)
	v_pk_add_f32 v[92:93], v[92:93], v[206:207]
	v_pk_add_f32 v[94:95], v[94:95], v[208:209]
	v_pk_add_f32 v[88:89], v[88:89], v[210:211]
	v_pk_add_f32 v[90:91], v[90:91], v[212:213]
	v_cvt_pk_bf16_f32 v92, v92, v93
	v_cvt_pk_bf16_f32 v93, v94, v95
	v_cvt_pk_bf16_f32 v94, v88, v89
	v_cvt_pk_bf16_f32 v95, v90, v91
	global_store_dwordx4 v[242:243], v[92:95], off
	global_load_dwordx4 v[206:209], v[232:233], off
	global_load_dwordx4 v[210:213], v[232:233], off offset:16
	s_waitcnt vmcnt(15)
	v_pk_add_f32 v[84:85], v[84:85], v[214:215]
	v_pk_add_f32 v[86:87], v[86:87], v[216:217]
	v_pk_add_f32 v[80:81], v[80:81], v[218:219]
	v_pk_add_f32 v[82:83], v[82:83], v[220:221]
	v_cvt_pk_bf16_f32 v84, v84, v85
	v_cvt_pk_bf16_f32 v85, v86, v87
	v_cvt_pk_bf16_f32 v86, v80, v81
	v_cvt_pk_bf16_f32 v87, v82, v83
	global_store_dwordx4 v[242:243], v[84:87], off offset:256
	global_load_dwordx4 v[214:217], v[232:233], off offset:512
	global_load_dwordx4 v[218:221], v[232:233], off offset:528
	s_waitcnt vmcnt(15)
	v_pk_add_f32 v[76:77], v[76:77], v[174:175]
	v_pk_add_f32 v[78:79], v[78:79], v[176:177]
	v_pk_add_f32 v[72:73], v[72:73], v[178:179]
	v_pk_add_f32 v[74:75], v[74:75], v[180:181]
	v_cvt_pk_bf16_f32 v76, v76, v77
	v_cvt_pk_bf16_f32 v77, v78, v79
	v_cvt_pk_bf16_f32 v78, v72, v73
	v_cvt_pk_bf16_f32 v79, v74, v75
	global_store_dwordx4 v[244:245], v[76:79], off
	global_load_dwordx4 v[174:177], v[234:235], off
	global_load_dwordx4 v[178:181], v[234:235], off offset:16
	s_waitcnt vmcnt(15)
	v_pk_add_f32 v[68:69], v[68:69], v[182:183]
	v_pk_add_f32 v[70:71], v[70:71], v[184:185]
	v_pk_add_f32 v[64:65], v[64:65], v[186:187]
	v_pk_add_f32 v[66:67], v[66:67], v[188:189]
	v_cvt_pk_bf16_f32 v68, v68, v69
	v_cvt_pk_bf16_f32 v69, v70, v71
	v_cvt_pk_bf16_f32 v70, v64, v65
	v_cvt_pk_bf16_f32 v71, v66, v67
	global_store_dwordx4 v[244:245], v[68:71], off offset:256
	global_load_dwordx4 v[182:185], v[234:235], off offset:512
	global_load_dwordx4 v[186:189], v[234:235], off offset:528
	s_waitcnt vmcnt(15)
	v_pk_add_f32 v[60:61], v[60:61], v[190:191]
	v_pk_add_f32 v[62:63], v[62:63], v[192:193]
	v_pk_add_f32 v[56:57], v[56:57], v[194:195]
	v_pk_add_f32 v[58:59], v[58:59], v[196:197]
	v_cvt_pk_bf16_f32 v60, v60, v61
	v_cvt_pk_bf16_f32 v61, v62, v63
	v_cvt_pk_bf16_f32 v62, v56, v57
	v_cvt_pk_bf16_f32 v63, v58, v59
	global_store_dwordx4 v[246:247], v[60:63], off
	global_load_dwordx4 v[190:193], v[236:237], off
	global_load_dwordx4 v[194:197], v[236:237], off offset:16
	s_waitcnt vmcnt(15)
	v_pk_add_f32 v[52:53], v[52:53], v[198:199]
	v_pk_add_f32 v[54:55], v[54:55], v[200:201]
	v_pk_add_f32 v[48:49], v[48:49], v[202:203]
	v_pk_add_f32 v[50:51], v[50:51], v[204:205]
	v_cvt_pk_bf16_f32 v52, v52, v53
	v_cvt_pk_bf16_f32 v53, v54, v55
	v_cvt_pk_bf16_f32 v54, v48, v49
	v_cvt_pk_bf16_f32 v55, v50, v51
	global_store_dwordx4 v[246:247], v[52:55], off offset:256
	global_load_dwordx4 v[198:201], v[236:237], off offset:512
	global_load_dwordx4 v[202:205], v[236:237], off offset:528
	s_waitcnt vmcnt(15)
	v_pk_add_f32 v[44:45], v[44:45], v[206:207]
	v_pk_add_f32 v[46:47], v[46:47], v[208:209]
	v_pk_add_f32 v[40:41], v[40:41], v[210:211]
	v_pk_add_f32 v[42:43], v[42:43], v[212:213]
	v_cvt_pk_bf16_f32 v44, v44, v45
	v_cvt_pk_bf16_f32 v45, v46, v47
	v_cvt_pk_bf16_f32 v46, v40, v41
	v_cvt_pk_bf16_f32 v47, v42, v43
	global_store_dwordx4 v[248:249], v[44:47], off
	s_waitcnt vmcnt(13)
	v_pk_add_f32 v[36:37], v[36:37], v[214:215]
	v_pk_add_f32 v[38:39], v[38:39], v[216:217]
	v_pk_add_f32 v[32:33], v[32:33], v[218:219]
	v_pk_add_f32 v[34:35], v[34:35], v[220:221]
	v_cvt_pk_bf16_f32 v36, v36, v37
	v_cvt_pk_bf16_f32 v37, v38, v39
	v_cvt_pk_bf16_f32 v38, v32, v33
	v_cvt_pk_bf16_f32 v39, v34, v35
	global_store_dwordx4 v[248:249], v[36:39], off offset:256
	s_waitcnt vmcnt(11)
	v_pk_add_f32 v[28:29], v[28:29], v[174:175]
	v_pk_add_f32 v[30:31], v[30:31], v[176:177]
	v_pk_add_f32 v[24:25], v[24:25], v[178:179]
	v_pk_add_f32 v[26:27], v[26:27], v[180:181]
	v_cvt_pk_bf16_f32 v28, v28, v29
	v_cvt_pk_bf16_f32 v29, v30, v31
	v_cvt_pk_bf16_f32 v30, v24, v25
	v_cvt_pk_bf16_f32 v31, v26, v27
	global_store_dwordx4 v[250:251], v[28:31], off
	s_waitcnt vmcnt(9)
	v_pk_add_f32 v[20:21], v[20:21], v[182:183]
	v_pk_add_f32 v[22:23], v[22:23], v[184:185]
	v_pk_add_f32 v[16:17], v[16:17], v[186:187]
	v_pk_add_f32 v[18:19], v[18:19], v[188:189]
	v_cvt_pk_bf16_f32 v20, v20, v21
	v_cvt_pk_bf16_f32 v21, v22, v23
	v_cvt_pk_bf16_f32 v22, v16, v17
	v_cvt_pk_bf16_f32 v23, v18, v19
	global_store_dwordx4 v[250:251], v[20:23], off offset:256
	s_waitcnt vmcnt(7)
	v_pk_add_f32 v[12:13], v[12:13], v[190:191]
	v_pk_add_f32 v[14:15], v[14:15], v[192:193]
	v_pk_add_f32 v[8:9], v[8:9], v[194:195]
	v_pk_add_f32 v[10:11], v[10:11], v[196:197]
	v_cvt_pk_bf16_f32 v12, v12, v13
	v_cvt_pk_bf16_f32 v13, v14, v15
	v_cvt_pk_bf16_f32 v14, v8, v9
	v_cvt_pk_bf16_f32 v15, v10, v11
	global_store_dwordx4 v[252:253], v[12:15], off
	s_waitcnt vmcnt(5)
	v_pk_add_f32 v[4:5], v[4:5], v[198:199]
	v_pk_add_f32 v[6:7], v[6:7], v[200:201]
	v_pk_add_f32 v[0:1], v[0:1], v[202:203]
	v_pk_add_f32 v[2:3], v[2:3], v[204:205]
	v_cvt_pk_bf16_f32 v4, v4, v5
	v_cvt_pk_bf16_f32 v5, v6, v7
	v_cvt_pk_bf16_f32 v6, v0, v1
	v_cvt_pk_bf16_f32 v7, v2, v3
	global_store_dwordx4 v[252:253], v[4:7], off offset:256
	s_cbranch_vccnz .LBB0_401
	s_andn2_b64 vcc, exec, s[6:7]
	s_cbranch_vccnz .LBB0_400
	s_barrier
	s_branch .LBB0_400
